# code placement: 4-byte pads at the starts of phases 8, 9 and 13 so that all six GEMM K-loop heads sit at 0 mod 8 bytes (P8 and P13 were at 4 mod 8)
# speedup vs baseline: 1.0059x; 1.0013x over previous
.LBB0_1796:
	s_nop 0
	s_cmp_lt_i32 s46, 9
	s_cselect_b64 s[6:7], -1, 0
	s_and_b64 s[12:13], s[6:7], s[4:5]
	s_andn2_b64 vcc, exec, s[12:13]
	s_cbranch_vccnz .LBB0_1974
	s_mov_b64 s[4:5], s[0:1]
	s_cmpk_lt_i32 s2, 0x400
	v_mov_b32_e32 v1, v0
	s_cselect_b64 s[4:5], -1, 0
	s_cmpk_gt_i32 s2, 0x3ff
	v_readfirstlane_b32 s20, v0
	s_cbranch_scc1 .LBB0_1803
	s_ashr_i32 s3, s2, 31
	s_lshr_b32 s3, s3, 29
	s_add_i32 s9, s2, s3
	s_and_b32 s3, s9, -8
	s_sub_i32 s3, s2, s3
	s_cmp_gt_i32 s3, -1
	s_cbranch_scc0 .LBB0_1800
	s_lshl_b32 s8, s3, 7
	s_ashr_i32 s6, s9, 3
	s_cbranch_execz .LBB0_1801
	s_branch .LBB0_1802

.LBB0_2024:
	s_nop 0
	s_cmp_lt_i32 s46, 10
	s_cselect_b64 s[6:7], -1, 0
	s_and_b64 s[12:13], s[6:7], s[4:5]
	s_andn2_b64 vcc, exec, s[12:13]
	s_cbranch_vccnz .LBB0_2097
	s_ashr_i32 s3, s2, 31
	s_mov_b64 s[4:5], s[0:1]
	v_mov_b32_e32 v2, v0
	v_mov_b64_e32 v[4:5], s[2:3]
	v_mov_b32_e32 v1, 0x400
	v_mad_i64_i32 v[4:5], s[4:5], v2, s48, v[4:5]
	s_mov_b64 s[4:5], 0x400
	s_nop 0
	v_cmp_lt_i64_e32 vcc, s[4:5], v[4:5]
	s_ashr_i32 s49, s48, 31
	s_mov_b32 s6, 0
	v_cndmask_b32_e32 v3, 0, v5, vcc
	v_cndmask_b32_e32 v1, v1, v4, vcc
	v_cmp_gt_i64_e32 vcc, s[4:5], v[4:5]
	v_mov_b32_e32 v7, s6
	s_lshl_b64 s[8:9], s[48:49], 9
	v_cndmask_b32_e64 v6, 0, 1, vcc
	v_lshl_add_u64 v[8:9], v[4:5], 0, v[6:7]
	v_cmp_gt_u64_e64 s[4:5], s[8:9], 1
	v_sub_co_u32_e32 v1, vcc, v1, v8
	s_and_b64 s[4:5], s[4:5], exec
	s_nop 0
	v_subb_co_u32_e32 v3, vcc, v3, v9, vcc
	s_cselect_b32 s11, s9, 0
	v_or_b32_e32 v9, s11, v3
	v_mov_b32_e32 v8, 0
	s_cselect_b32 s10, s8, 1
	v_cmp_ne_u64_e32 vcc, 0, v[8:9]
	s_waitcnt vmcnt(0) lgkmcnt(0)
	s_barrier
	s_and_saveexec_b64 s[4:5], vcc
	s_xor_b64 s[6:7], exec, s[4:5]
	s_cbranch_execz .LBB0_2027
	v_cvt_f32_u32_e32 v9, s10
	v_cvt_f32_u32_e32 v10, s11
	s_sub_u32 s14, 0, s10
	s_subb_u32 s15, 0, s11
	v_mov_b32_e32 v13, v8
	v_fmamk_f32 v9, v10, 0x4f800000, v9
	v_rcp_f32_e32 v9, v9
	s_nop 0
	v_mul_f32_e32 v9, 0x5f7ffffc, v9
	v_mul_f32_e32 v10, 0x2f800000, v9
	v_trunc_f32_e32 v10, v10
	v_fmamk_f32 v9, v10, 0xcf800000, v9
	v_cvt_u32_f32_e32 v10, v10
	v_cvt_u32_f32_e32 v9, v9
	v_readfirstlane_b32 s16, v10
	v_readfirstlane_b32 s4, v9
	s_mul_i32 s5, s14, s16
	s_mul_hi_u32 s18, s14, s4
	s_mul_i32 s17, s15, s4
	s_add_i32 s5, s18, s5
	s_mul_i32 s19, s14, s4
	s_add_i32 s5, s5, s17
	s_mul_i32 s18, s4, s5
	s_mul_hi_u32 s20, s4, s19
	s_mul_hi_u32 s17, s4, s5
	s_add_u32 s18, s20, s18
	s_addc_u32 s17, 0, s17
	s_mul_hi_u32 s21, s16, s19
	s_mul_i32 s19, s16, s19
	s_add_u32 s18, s18, s19
	s_mul_hi_u32 s20, s16, s5
	s_addc_u32 s17, s17, s21
	s_addc_u32 s18, s20, 0
	s_mul_i32 s5, s16, s5
	s_add_u32 s5, s17, s5
	s_addc_u32 s17, 0, s18
	s_add_u32 s18, s4, s5
	s_cselect_b64 s[4:5], -1, 0
	s_cmp_lg_u64 s[4:5], 0
	s_addc_u32 s16, s16, s17
	s_mul_i32 s4, s14, s16
	s_mul_hi_u32 s5, s14, s18
	s_add_i32 s4, s5, s4
	s_mul_i32 s15, s15, s18
	s_add_i32 s4, s4, s15
	s_mul_i32 s14, s14, s18
	s_mul_hi_u32 s15, s16, s14
	s_mul_i32 s17, s16, s14
	s_mul_i32 s20, s18, s4
	s_mul_hi_u32 s14, s18, s14
	s_mul_hi_u32 s19, s18, s4
	s_add_u32 s14, s14, s20
	s_addc_u32 s19, 0, s19
	s_add_u32 s14, s14, s17
	s_mul_hi_u32 s5, s16, s4
	s_addc_u32 s14, s19, s15
	s_addc_u32 s5, s5, 0
	s_mul_i32 s4, s16, s4
	s_add_u32 s4, s14, s4
	s_addc_u32 s14, 0, s5
	s_add_u32 s15, s18, s4
	s_cselect_b64 s[4:5], -1, 0
	s_cmp_lg_u64 s[4:5], 0
	s_addc_u32 s14, s16, s14
	v_mad_u64_u32 v[10:11], s[4:5], v1, s14, 0
	v_mul_hi_u32 v12, v1, s15
	v_lshl_add_u64 v[10:11], v[12:13], 0, v[10:11]
	v_mad_u64_u32 v[14:15], s[4:5], v3, s15, 0
	v_add_co_u32_e32 v9, vcc, v10, v14
	v_mad_u64_u32 v[12:13], s[4:5], v3, s14, 0
	s_nop 0
	v_addc_co_u32_e32 v10, vcc, v11, v15, vcc
	v_mov_b32_e32 v11, v8
	s_nop 0
	v_addc_co_u32_e32 v13, vcc, 0, v13, vcc
	v_lshl_add_u64 v[8:9], v[10:11], 0, v[12:13]
	v_mul_lo_u32 v12, s11, v8
	v_mul_lo_u32 v13, s10, v9
	v_mad_u64_u32 v[10:11], s[4:5], s10, v8, 0
	v_add3_u32 v14, v11, v13, v12
	v_sub_u32_e32 v11, v3, v14
	v_mov_b32_e32 v12, s11
	v_sub_co_u32_e32 v1, vcc, v1, v10
	s_nop 1
	v_subb_co_u32_e64 v10, s[4:5], v11, v12, vcc
	v_subrev_co_u32_e64 v11, s[4:5], s10, v1
	v_subb_co_u32_e32 v3, vcc, v3, v14, vcc
	s_nop 0
	v_subbrev_co_u32_e64 v10, s[4:5], 0, v10, s[4:5]
	v_cmp_le_u32_e64 s[4:5], s11, v10
	v_cmp_le_u32_e32 vcc, s11, v3
	s_nop 0
	v_cndmask_b32_e64 v12, 0, -1, s[4:5]
	v_cmp_le_u32_e64 s[4:5], s10, v11
	s_nop 1
	v_cndmask_b32_e64 v11, 0, -1, s[4:5]
	v_cmp_eq_u32_e64 s[4:5], s11, v10
	s_nop 1
	v_cndmask_b32_e64 v15, v12, v11, s[4:5]
	v_lshl_add_u64 v[10:11], v[8:9], 0, 2
	v_lshl_add_u64 v[12:13], v[8:9], 0, 1
	v_cmp_ne_u32_e64 s[4:5], 0, v15
	s_nop 1
	v_cndmask_b32_e64 v11, v13, v11, s[4:5]
	v_cndmask_b32_e64 v13, 0, -1, vcc
	v_cmp_le_u32_e32 vcc, s10, v1
	s_nop 1
	v_cndmask_b32_e64 v1, 0, -1, vcc
	v_cmp_eq_u32_e32 vcc, s11, v3
	s_nop 1
	v_cndmask_b32_e32 v1, v13, v1, vcc
	v_cmp_ne_u32_e32 vcc, 0, v1
	v_cndmask_b32_e64 v1, v12, v10, s[4:5]
	s_nop 0
	v_cndmask_b32_e32 v11, v9, v11, vcc
	v_cndmask_b32_e32 v10, v8, v1, vcc

.LBB0_2393:
	s_nop 0
	s_cmp_lt_i32 s46, 14
	s_cselect_b64 s[8:9], -1, 0
	s_and_b64 s[16:17], s[8:9], s[4:5]
	s_andn2_b64 vcc, exec, s[16:17]
	s_cbranch_vccnz .LBB0_2465
	s_mov_b64 s[4:5], s[0:1]
	v_mov_b32_e32 v3, v0
	s_andn2_b64 vcc, exec, s[6:7]
	s_cbranch_vccnz .LBB0_2400
	v_lshlrev_b32_e32 v1, 4, v3
	v_and_b32_e32 v4, 0xfffffe00, v1
	v_ashrrev_i32_e32 v5, 31, v4
	v_lshlrev_b32_e32 v1, 2, v3
	v_lshl_add_u64 v[4:5], v[4:5], 2, s[44:45]
	v_and_b32_e32 v6, 0x7c, v1
	v_mov_b32_e32 v7, 0
	v_lshl_add_u64 v[4:5], v[4:5], 0, v[6:7]
	s_mov_b64 s[6:7], 0x40f80000
	s_mov_b32 s3, 0x40f80000
	v_lshl_add_u64 v[8:9], v[4:5], 0, s[6:7]
	v_add_co_u32_e32 v4, vcc, s3, v4
	s_waitcnt vmcnt(0) lgkmcnt(0)
	s_barrier
	v_addc_co_u32_e32 v5, vcc, 0, v5, vcc
	global_load_dword v2, v[8:9], off offset:128
	global_load_dword v7, v[8:9], off offset:256
	global_load_dword v10, v[8:9], off offset:384
	global_load_dword v11, v[8:9], off offset:512
	global_load_dword v12, v[8:9], off offset:640
	global_load_dword v13, v[8:9], off offset:768
	global_load_dword v14, v[8:9], off offset:896
	global_load_dword v15, v[8:9], off offset:1024
	global_load_dword v16, v[4:5], off
	global_load_dword v17, v[8:9], off offset:1152
	global_load_dword v18, v[8:9], off offset:1280
	global_load_dword v19, v[8:9], off offset:1408
	global_load_dword v20, v[8:9], off offset:1536
	global_load_dword v21, v[8:9], off offset:1664
	global_load_dword v22, v[8:9], off offset:1792
	global_load_dword v4, v[8:9], off offset:1920
	v_and_b32_e32 v8, 0x3fffffe0, v3
	s_add_i32 s3, 0, 0x21000
	v_ashrrev_i32_e32 v5, 31, v3
	v_add_u32_e32 v1, s3, v1
	v_lshlrev_b32_e32 v8, 2, v8
	v_cmp_gt_i32_e32 vcc, 32, v3
	v_add3_u32 v6, s3, v8, v6
	s_waitcnt vmcnt(7)
	v_add_u32_e32 v2, v2, v16
	v_add3_u32 v2, v2, v7, v10
	v_add3_u32 v2, v2, v11, v12
	v_add3_u32 v2, v2, v13, v14
	s_waitcnt vmcnt(6)
	v_add3_u32 v2, v2, v15, v17
	s_waitcnt vmcnt(4)
	v_add3_u32 v2, v2, v18, v19
	s_waitcnt vmcnt(2)
	v_add3_u32 v2, v2, v20, v21
	s_waitcnt vmcnt(0)
	v_add3_u32 v2, v2, v22, v4
	v_and_b32_e32 v4, v5, v2
	ds_write_b32 v1, v2
	ds_write_b32 v6, v4 offset:2048
	s_waitcnt lgkmcnt(0)
	s_barrier
	s_and_saveexec_b64 s[6:7], vcc
	s_cbranch_execz .LBB0_2397
	v_lshl_add_u32 v2, v3, 2, 0
	v_add_u32_e32 v4, 0x21800, v2
	v_add_u32_e32 v5, 0x21080, v2
	v_add_u32_e32 v6, 0x21880, v2
	v_add_u32_e32 v7, 0x21100, v2
	v_add_u32_e32 v8, 0x21900, v2
	v_add_u32_e32 v9, 0x21180, v2
	v_add_u32_e32 v10, 0x21980, v2
	ds_read_b32 v1, v1
	ds_read_b32 v4, v4
	ds_read_b32 v5, v5
	ds_read_b32 v6, v6
	ds_read_b32 v7, v7
	ds_read_b32 v9, v9
	ds_read_b32 v8, v8
	ds_read_b32 v10, v10
	s_waitcnt lgkmcnt(5)
	v_add_u32_e32 v1, v5, v1
	s_waitcnt lgkmcnt(4)
	v_add_u32_e32 v4, v6, v4
	s_waitcnt lgkmcnt(2)
	v_add3_u32 v1, v1, v7, v9
	v_add_u32_e32 v5, 0x21200, v2
	v_add_u32_e32 v6, 0x21a00, v2
	v_add_u32_e32 v7, 0x21280, v2
	v_add_u32_e32 v9, 0x21a80, v2
	v_add_u32_e32 v11, 0x21300, v2
	v_add_u32_e32 v12, 0x21b00, v2
	v_add_u32_e32 v13, 0x21380, v2
	v_add_u32_e32 v14, 0x21b80, v2
	ds_read_b32 v5, v5
	ds_read_b32 v6, v6
	ds_read_b32 v7, v7
	ds_read_b32 v9, v9
	ds_read_b32 v11, v11
	ds_read_b32 v12, v12
	ds_read_b32 v13, v13
	ds_read_b32 v14, v14
	s_waitcnt lgkmcnt(8)
	v_add3_u32 v4, v4, v8, v10
	s_waitcnt lgkmcnt(5)
	v_add3_u32 v1, v1, v5, v7
	s_waitcnt lgkmcnt(4)
	v_add3_u32 v4, v4, v6, v9
	s_waitcnt lgkmcnt(1)
	v_add3_u32 v1, v1, v11, v13
	s_waitcnt lgkmcnt(0)
	v_add3_u32 v4, v4, v12, v14
	v_add_u32_e32 v5, 0x21400, v2
	v_add_u32_e32 v6, 0x21c00, v2
	v_add_u32_e32 v7, 0x21480, v2
	v_add_u32_e32 v8, 0x21c80, v2
	v_add_u32_e32 v9, 0x21500, v2
	v_add_u32_e32 v10, 0x21d00, v2
	v_add_u32_e32 v11, 0x21580, v2
	v_add_u32_e32 v12, 0x21d80, v2
	ds_read_b32 v5, v5
	ds_read_b32 v6, v6
	ds_read_b32 v7, v7
	ds_read_b32 v8, v8
	ds_read_b32 v9, v9
	ds_read_b32 v11, v11
	ds_read_b32 v10, v10
	ds_read_b32 v12, v12
	s_waitcnt lgkmcnt(5)
	v_add3_u32 v1, v1, v5, v7
	s_waitcnt lgkmcnt(4)
	v_add3_u32 v4, v4, v6, v8
	s_waitcnt lgkmcnt(2)
	v_add3_u32 v1, v1, v9, v11
	v_add_u32_e32 v5, 0x21600, v2
	v_add_u32_e32 v6, 0x21e00, v2
	v_add_u32_e32 v7, 0x21680, v2
	v_add_u32_e32 v8, 0x21e80, v2
	v_add_u32_e32 v9, 0x21700, v2
	v_add_u32_e32 v11, 0x21f00, v2
	v_add_u32_e32 v13, 0x21780, v2
	v_add_u32_e32 v14, 0x21f80, v2
	ds_read_b32 v5, v5
	ds_read_b32 v6, v6
	ds_read_b32 v7, v7
	ds_read_b32 v8, v8
	ds_read_b32 v9, v9
	ds_read_b32 v11, v11
	ds_read_b32 v13, v13
	ds_read_b32 v14, v14
	s_waitcnt lgkmcnt(8)
	v_add3_u32 v4, v4, v10, v12
	s_waitcnt lgkmcnt(5)
	v_add3_u32 v1, v1, v5, v7
	s_waitcnt lgkmcnt(4)
	v_add3_u32 v4, v4, v6, v8
	s_waitcnt lgkmcnt(1)
	v_add3_u32 v1, v1, v9, v13
	s_waitcnt lgkmcnt(0)
	v_add3_u32 v4, v4, v11, v14
	v_add_u32_e32 v2, 0x20000, v2
	ds_write_b32 v2, v4 offset:640
	v_add_u32_e32 v4, 0xff, v1
	v_ashrrev_i32_e32 v4, 8, v4
	ds_write2st64_b32 v2, v1, v4 offset1:1
